# v24: v22 + first kernarg s_load hoisted to the very first instruction of each kernel
# speedup vs baseline: 1.0110x; 1.0110x over previous
_Z7k_pointPDF16_S_S_PKfS1_S1_S1_S1_S1_S1_S1_S1_S1_S1_S1_S1_S1_:
	s_load_dwordx16 s[60:75], s[0:1], 0x0
	s_load_dwordx16 s[76:91], s[0:1], 0x40
	s_load_dwordx2 s[92:93], s[0:1], 0x80
	v_bfe_u32 v105, v0, 6, 2
	v_lshrrev_b32_e32 v104, 8, v0
	v_lshlrev_b32_e32 v1, 4, v105
	v_lshl_or_b32 v14, s2, 6, v1
	v_lshlrev_b32_e32 v107, 3, v104
	v_or_b32_e32 v2, v14, v107
	v_lshlrev_b32_e32 v2, 6, v2
	v_ashrrev_i32_e32 v3, 31, v2
	v_and_b32_e32 v103, 63, v0
	v_lshlrev_b64 v[2:3], 2, v[2:3]
	s_waitcnt lgkmcnt(0)
	v_lshl_add_u64 v[4:5], s[68:69], 0, v[2:3]
	v_lshlrev_b32_e32 v94, 4, v103
	v_mov_b32_e32 v95, 0
	v_lshl_add_u64 v[4:5], v[4:5], 0, v[94:95]
	v_lshl_add_u64 v[2:3], s[70:71], 0, v[2:3]
	v_mul_u32_u24_e32 v113, 0xe39, v0
	s_movk_i32 s2, 0xffee
	v_lshl_add_u64 v[2:3], v[2:3], 0, v[94:95]
	global_load_dwordx4 v[58:61], v[4:5], off nt
	global_load_dwordx4 v[50:53], v[4:5], off offset:1024 nt
	global_load_dwordx4 v[62:65], v[2:3], off nt
	global_load_dwordx4 v[54:57], v[2:3], off offset:1024 nt
	v_mul_i32_i24_sdwa v4, v113, s2 dst_sel:DWORD dst_unused:UNUSED_PAD src0_sel:WORD_1 src1_sel:DWORD
	s_movk_i32 s3, 0x48
	v_mul_u32_u24_sdwa v2, v113, s3 dst_sel:DWORD dst_unused:UNUSED_PAD src0_sel:WORD_1 src1_sel:DWORD
	v_add_lshl_u32 v96, v4, v0, 2
	v_lshlrev_b32_e32 v2, 2, v2
	v_mov_b32_e32 v3, v95
	v_ashrrev_i32_e32 v97, 31, v96
	v_lshl_add_u64 v[6:7], s[74:75], 0, v[2:3]
	v_lshlrev_b64 v[4:5], 2, v[96:97]
	v_or_b32_e32 v8, 0x200, v0
	v_lshl_add_u64 v[10:11], v[6:7], 0, v[4:5]
	v_mul_u32_u24_e32 v6, 0xe39, v8
	v_mul_i32_i24_sdwa v9, v6, s2 dst_sel:DWORD dst_unused:UNUSED_PAD src0_sel:WORD_1 src1_sel:DWORD
	v_mul_u32_u24_sdwa v6, v6, s3 dst_sel:DWORD dst_unused:UNUSED_PAD src0_sel:WORD_1 src1_sel:DWORD
	v_add_lshl_u32 v8, v9, v8, 2
	v_lshlrev_b32_e32 v6, 2, v6
	v_mov_b32_e32 v7, v95
	v_ashrrev_i32_e32 v9, 31, v8
	v_lshl_add_u64 v[12:13], s[74:75], 0, v[6:7]
	v_lshlrev_b64 v[8:9], 2, v[8:9]
	v_lshl_add_u64 v[12:13], v[12:13], 0, v[8:9]
	v_or_b32_e32 v106, 0x400, v0
	global_load_dwordx4 v[90:93], v[10:11], off
	global_load_dwordx4 v[86:89], v[12:13], off
	v_min_u32_e32 v12, 0x50f, v106
	v_mul_u32_u24_e32 v15, 0xe39, v12
	v_mul_i32_i24_sdwa v13, v15, s2 dst_sel:DWORD dst_unused:UNUSED_PAD src0_sel:WORD_1 src1_sel:DWORD
	v_mul_u32_u24_sdwa v10, v15, s3 dst_sel:DWORD dst_unused:UNUSED_PAD src0_sel:WORD_1 src1_sel:DWORD
	v_add_lshl_u32 v12, v13, v12, 2
	v_lshlrev_b32_e32 v98, 2, v10
	v_mov_b32_e32 v99, v95
	v_ashrrev_i32_e32 v13, 31, v12
	v_lshl_add_u64 v[10:11], s[74:75], 0, v[98:99]
	v_lshlrev_b64 v[100:101], 2, v[12:13]
	v_lshl_add_u64 v[10:11], v[10:11], 0, v[100:101]
	s_movk_i32 s2, 0x42
	global_load_dwordx4 v[82:85], v[10:11], off
	v_lshl_add_u64 v[10:11], s[78:79], 0, v[2:3]
	v_min_u32_sdwa v3, v15, s2 dst_sel:DWORD dst_unused:UNUSED_PAD src0_sel:WORD_1 src1_sel:DWORD
	v_lshl_add_u64 v[10:11], v[10:11], 0, v[4:5]
	v_lshl_add_u64 v[12:13], s[78:79], 0, v[6:7]
	v_mul_u32_u24_e32 v3, 0x48, v3
	v_lshl_add_u64 v[12:13], v[12:13], 0, v[8:9]
	global_load_dwordx4 v[74:77], v[10:11], off
	global_load_dwordx4 v[78:81], v[12:13], off
	v_lshlrev_b32_e32 v10, 2, v3
	v_mov_b32_e32 v11, v95
	v_lshl_add_u64 v[10:11], s[78:79], 0, v[10:11]
	v_min_u32_e32 v3, 0x47, v0
	v_lshl_add_u64 v[10:11], v[10:11], 0, v[100:101]
	v_lshlrev_b32_e32 v3, 2, v3
	global_load_dwordx4 v[70:73], v[10:11], off
	global_load_dword v109, v3, s[76:77]
	global_load_dword v110, v3, s[80:81]
	global_load_dword v111, v3, s[84:85]
	global_load_dword v112, v3, s[90:91]
	s_movk_i32 s2, 0x100
	v_and_b32_e32 v102, 15, v0
	v_cmp_gt_u32_e32 vcc, s2, v0
	s_movk_i32 s2, 0xff
	v_or_b32_e32 v97, v14, v102
	v_cmp_lt_u32_e64 s[4:5], s2, v0
	s_and_saveexec_b64 s[2:3], s[4:5]
	s_xor_b64 s[6:7], exec, s[2:3]
	s_cbranch_execz .LBB0_2
	v_lshl_add_u32 v10, v97, 1, v97
	v_ashrrev_i32_e32 v11, 31, v10
	v_mov_b32_e32 v69, v95
	v_lshl_add_u64 v[10:11], v[10:11], 2, s[66:67]
	global_load_dwordx3 v[66:68], v[10:11], off nt

_Z5k_ncaILi0EEvPKDF16_S1_PKfS3_PDF16_S3_S3_S3_S3_Pf:
	s_load_dwordx4 s[12:15], s[0:1], 0x0
	s_lshl_b32 s3, s2, 1
	s_and_b32 s3, s3, 12
	s_lshr_b32 s4, s2, 6
	v_lshrrev_b32_e32 v1, 5, v0
	s_add_i32 s3, s3, s4
	s_lshl_b32 s4, s2, 6
	v_and_b32_e32 v62, 4, v1
	v_lshrrev_b32_e32 v1, 4, v0
	s_and_b32 s4, s4, 64
	s_and_b32 s2, s2, 56
	v_and_b32_e32 v63, 4, v1
	v_bfe_u32 v1, v0, 2, 2
	s_lshl_b32 s20, s3, 3
	s_or_b32 s21, s4, s2
	v_or3_b32 v2, v62, s20, v1
	v_and_b32_e32 v61, 3, v0
	v_lshl_or_b32 v2, v2, 7, s21
	v_or3_b32 v2, v2, v63, v61
	s_movk_i32 s4, 0x48
	v_mul_lo_u32 v54, v2, s4
	v_mov_b32_e32 v55, 0
	s_waitcnt lgkmcnt(0)
	v_lshl_add_u64 v[6:7], v[54:55], 1, s[12:13]
	v_and_b32_e32 v2, 48, v0
	v_mov_b32_e32 v3, v55
	v_lshl_add_u64 v[8:9], v[6:7], 0, v[2:3]
	global_load_dwordx4 v[2:5], v[8:9], off offset:64
	global_load_dwordx4 v[10:13], v[8:9], off
	global_load_dwordx4 v[22:25], v[6:7], off offset:128
	v_mul_u32_u24_e32 v6, 0x1c72, v0
	v_mul_u32_u24_e32 v65, 0x195, v0
	s_movk_i32 s2, 0xffee
	s_add_i32 s20, s20, -5
	s_add_i32 s21, s21, -5
	v_lshrrev_b32_e32 v64, 16, v6
	v_mul_i32_i24_sdwa v6, v65, s2 dst_sel:DWORD dst_unused:UNUSED_PAD src0_sel:WORD_1 src1_sel:DWORD
	v_add_u32_sdwa v14, s20, v65 dst_sel:DWORD dst_unused:UNUSED_PAD src0_sel:DWORD src1_sel:WORD_1
	v_add3_u32 v15, s21, v64, v6
	v_or_b32_e32 v6, v15, v14
	s_movk_i32 s5, 0x80
	v_cmp_gt_u32_e32 vcc, s5, v6
	v_mov_b64_e32 v[6:7], 0
	v_mov_b64_e32 v[8:9], 0
	s_and_saveexec_b64 s[2:3], vcc
	v_lshl_or_b32 v9, v14, 7, v15
	v_mad_i32_i24 v8, v64, -9, v0
	v_mul_lo_u32 v9, v9, s4
	v_lshl_add_u32 v8, v8, 3, v9
	v_ashrrev_i32_e32 v9, 31, v8
	s_or_b64 exec, exec, s[2:3]
	v_lshl_add_u64 v[8:9], v[8:9], 1, s[14:15]
	global_load_dwordx4 v[26:29], v[8:9], off
	v_or_b32_e32 v59, 0x200, v0
	v_mul_u32_u24_e32 v8, 0x1c72, v59
	v_lshrrev_b32_e32 v66, 16, v8
	v_mul_u32_u24_e32 v8, 0x653, v59
	v_lshrrev_b32_e32 v67, 18, v8
	v_mul_i32_i24_e32 v9, 0xffffffee, v67
	v_add_u32_e32 v8, s20, v67
	v_add3_u32 v9, s21, v66, v9
	v_or_b32_e32 v14, v9, v8
	v_cmp_gt_u32_e64 s[2:3], s5, v14
	s_and_saveexec_b64 s[4:5], s[2:3]
	v_lshl_or_b32 v7, v8, 7, v9
	s_movk_i32 s6, 0x48
	v_mad_i32_i24 v6, v66, -9, v59
	v_mul_lo_u32 v7, v7, s6
	v_lshl_add_u32 v6, v6, 3, v7
	v_ashrrev_i32_e32 v7, 31, v6
	s_or_b64 exec, exec, s[4:5]
	v_lshl_add_u64 v[6:7], v[6:7], 1, s[14:15]
	global_load_dwordx4 v[30:33], v[6:7], off
	v_or_b32_e32 v58, 0x400, v0
	v_mul_u32_u24_e32 v6, 0x1c72, v58
	v_lshrrev_b32_e32 v68, 16, v6
	v_mul_u32_u24_e32 v6, 0x653, v58
	v_lshrrev_b32_e32 v69, 18, v6
	v_mul_i32_i24_e32 v6, 0xffffffee, v69
	v_add_u32_e32 v14, s20, v69
	v_add3_u32 v15, s21, v68, v6
	v_or_b32_e32 v6, v15, v14
	s_movk_i32 s8, 0x80
	v_cmp_gt_u32_e64 s[4:5], s8, v6
	v_mov_b64_e32 v[6:7], 0
	v_mov_b64_e32 v[8:9], 0
	s_and_saveexec_b64 s[6:7], s[4:5]
	v_lshl_or_b32 v9, v14, 7, v15
	s_movk_i32 s9, 0x48
	v_mad_i32_i24 v8, v68, -9, v58
	v_mul_lo_u32 v9, v9, s9
	v_lshl_add_u32 v8, v8, 3, v9
	v_mov_b32_e32 v9, 0
	s_or_b64 exec, exec, s[6:7]
	v_lshl_add_u64 v[8:9], v[8:9], 1, s[14:15]
	global_load_dwordx4 v[34:37], v[8:9], off
	v_or_b32_e32 v70, 0x600, v0
	v_mul_u32_u24_e32 v8, 0x1c72, v70
	v_lshrrev_b32_e32 v71, 16, v8
	v_mul_u32_u24_e32 v8, 0x653, v70
	v_lshrrev_b32_e32 v72, 18, v8
	v_mul_i32_i24_e32 v9, 0xffffffee, v72
	v_add_u32_e32 v8, s20, v72
	v_add3_u32 v9, s21, v71, v9
	v_or_b32_e32 v14, v9, v8
	v_cmp_gt_u32_e64 s[8:9], s8, v14
	s_and_saveexec_b64 s[6:7], s[8:9]
	v_lshl_or_b32 v7, v8, 7, v9
	s_movk_i32 s10, 0x48
	v_mad_i32_i24 v6, v71, -9, v70
	v_mul_lo_u32 v7, v7, s10
	v_lshl_add_u32 v6, v6, 3, v7
	v_mov_b32_e32 v7, 0
	s_or_b64 exec, exec, s[6:7]
	v_lshl_add_u64 v[6:7], v[6:7], 1, s[14:15]
	global_load_dwordx4 v[42:45], v[6:7], off
	v_or_b32_e32 v73, 0x800, v0
	v_mul_u32_u24_e32 v6, 0x1c72, v73
	v_lshrrev_b32_e32 v14, 16, v6
	v_mul_u32_u24_e32 v6, 0xca5, v73
	s_load_dwordx2 s[12:13], s[0:1], 0x18
	v_lshrrev_b32_e32 v6, 19, v6
	v_mul_i32_i24_e32 v7, 0xffffffee, v6
	v_add_u32_e32 v15, s20, v6
	v_add3_u32 v16, s21, v14, v7
	v_or_b32_e32 v6, v16, v15
	s_movk_i32 s18, 0x80
	v_cmp_gt_u32_e64 s[10:11], s18, v6
	v_mov_b64_e32 v[6:7], 0
	v_mov_b64_e32 v[8:9], 0
	s_and_saveexec_b64 s[6:7], s[10:11]
	v_lshl_or_b32 v9, v15, 7, v16
	s_movk_i32 s16, 0x48
	v_mad_i32_i24 v8, v14, -9, v73
	v_mul_lo_u32 v9, v9, s16
	v_lshl_add_u32 v8, v8, 3, v9
	v_mov_b32_e32 v9, 0
	s_or_b64 exec, exec, s[6:7]
	v_lshl_add_u64 v[8:9], v[8:9], 1, s[14:15]
	global_load_dwordx4 v[46:49], v[8:9], off
	v_or_b32_e32 v74, 0xa00, v0
	v_min_u32_e32 v8, 0xb63, v74
	v_mul_u32_u24_e32 v14, 0xca5, v8
	s_load_dwordx2 s[16:17], s[0:1], 0x10
	s_load_dwordx2 s[64:65], s[0:1], 0x20
	v_mul_u32_u24_e32 v9, 0x1c72, v8
	v_lshrrev_b32_e32 v14, 19, v14
	v_lshrrev_b32_e32 v9, 16, v9
	v_mul_i32_i24_e32 v15, 0xffffffee, v14
	v_add_u32_e32 v14, s20, v14
	v_add3_u32 v15, s21, v9, v15
	v_or_b32_e32 v16, v15, v14
	v_cmp_gt_u32_e64 s[6:7], s18, v16
	s_and_saveexec_b64 s[18:19], s[6:7]
	v_lshl_or_b32 v7, v14, 7, v15
	s_movk_i32 s22, 0x48
	v_mad_i32_i24 v6, v9, -9, v8
	v_mul_lo_u32 v7, v7, s22
	v_lshl_add_u32 v6, v6, 3, v7
	v_mov_b32_e32 v7, 0
	s_or_b64 exec, exec, s[18:19]
	v_lshl_add_u64 v[6:7], v[6:7], 1, s[14:15]
	s_movk_i32 s14, 0xe39
	global_load_dwordx4 v[38:41], v[6:7], off
	v_mul_u32_u24_sdwa v6, v0, s14 dst_sel:DWORD dst_unused:UNUSED_PAD src0_sel:WORD_0 src1_sel:DWORD
	v_lshrrev_b32_e32 v60, 16, v6
	v_or_b32_e32 v14, 0x200, v0
	s_movk_i32 s14, 0xffee
	s_movk_i32 s15, 0x48
	v_mul_u32_u24_e32 v6, 0x48, v60
	v_mul_u32_u24_e32 v8, 0xe39, v14
	v_mad_i32_i24 v52, v60, s14, v0
	v_lshlrev_b32_e32 v50, 2, v6
	v_mov_b32_e32 v51, 0
	v_mul_i32_i24_sdwa v15, v8, s14 dst_sel:DWORD dst_unused:UNUSED_PAD src0_sel:WORD_1 src1_sel:DWORD
	v_mul_u32_u24_sdwa v8, v8, s15 dst_sel:DWORD dst_unused:UNUSED_PAD src0_sel:WORD_1 src1_sel:DWORD
	s_waitcnt lgkmcnt(0)
	v_lshl_add_u64 v[6:7], s[16:17], 0, v[50:51]
	v_lshlrev_b32_e32 v56, 2, v52
	v_lshlrev_b32_e32 v50, 2, v8
	v_add_lshl_u32 v14, v15, v14, 2
	v_ashrrev_i32_e32 v57, 31, v56
	v_lshl_add_u64 v[8:9], s[16:17], 0, v[50:51]
	v_ashrrev_i32_e32 v15, 31, v14
	v_lshl_add_u64 v[6:7], v[56:57], 2, v[6:7]
	v_lshl_add_u64 v[8:9], v[14:15], 2, v[8:9]
	global_load_dwordx4 v[18:21], v[6:7], off
	global_load_dwordx4 v[14:17], v[8:9], off
	v_min_u32_e32 v8, 0x50f, v58
	v_mul_u32_u24_e32 v6, 0xe39, v8
	v_mul_i32_i24_sdwa v9, v6, s14 dst_sel:DWORD dst_unused:UNUSED_PAD src0_sel:WORD_1 src1_sel:DWORD
	v_mul_u32_u24_sdwa v6, v6, s15 dst_sel:DWORD dst_unused:UNUSED_PAD src0_sel:WORD_1 src1_sel:DWORD
	v_lshlrev_b32_e32 v50, 2, v6
	v_add_lshl_u32 v8, v9, v8, 2
	v_lshl_add_u64 v[6:7], s[16:17], 0, v[50:51]
	v_ashrrev_i32_e32 v9, 31, v8
	v_min_u32_e32 v50, 0x47, v0
	v_lshl_add_u64 v[6:7], v[8:9], 2, v[6:7]
	v_lshlrev_b32_e32 v50, 2, v50
	global_load_dwordx4 v[6:9], v[6:7], off
	s_nop 0
	global_load_dword v57, v50, s[12:13]
	s_movk_i32 s12, 0x144
	v_cmp_gt_u32_e64 s[12:13], s12, v0
	s_and_saveexec_b64 s[14:15], s[12:13]
	s_cbranch_execz .LBB1_14
	v_mul_i32_i24_e32 v50, 0x1c72, v52
	v_lshrrev_b32_e32 v53, 31, v50
	v_add_u16_sdwa v50, v50, v53 dst_sel:DWORD dst_unused:UNUSED_PAD src0_sel:WORD_1 src1_sel:DWORD
	v_bfe_i32 v50, v50, 0, 16
	v_mul_i32_i24_e32 v53, -9, v50
	v_mad_u32_u24 v50, v60, 20, v50
	v_mul_i32_i24_e32 v50, 0xa0, v50
	v_add_lshl_u32 v52, v53, v52, 4
	v_add3_u32 v75, v50, 0, v52
	v_mov_b32_e32 v50, v51
	v_mov_b32_e32 v52, v51
	v_mov_b32_e32 v53, v51
	ds_write_b128 v75, v[50:53] offset:2880

_Z5k_ncaILi1EEvPKDF16_S1_PKfS3_PDF16_S3_S3_S3_S3_Pf:
	s_load_dwordx4 s[20:23], s[0:1], 0x0
	s_lshl_b32 s3, s2, 1
	s_and_b32 s3, s3, 12
	s_lshr_b32 s4, s2, 6
	s_add_i32 s3, s3, s4
	v_lshrrev_b32_e32 v1, 5, v0
	s_lshl_b32 s4, s2, 6
	v_and_b32_e32 v76, 4, v1
	s_lshl_b32 s29, s3, 3
	s_and_b32 s4, s4, 64
	s_and_b32 s2, s2, 56
	v_bfe_u32 v60, v0, 2, 2
	v_or_b32_e32 v58, s29, v76
	s_or_b32 s28, s4, s2
	v_lshrrev_b32_e32 v52, 4, v0
	v_or_b32_e32 v2, v58, v60
	v_and_b32_e32 v57, 4, v52
	v_and_b32_e32 v1, 3, v0
	v_lshl_or_b32 v2, v2, 7, s28
	v_or3_b32 v56, v2, v57, v1
	s_movk_i32 s4, 0x48
	v_mul_lo_u32 v2, v56, s4
	v_mov_b32_e32 v3, 0
	s_waitcnt lgkmcnt(0)
	v_lshl_add_u64 v[6:7], v[2:3], 1, s[20:21]
	v_and_b32_e32 v2, 48, v0
	v_lshl_add_u64 v[8:9], v[6:7], 0, v[2:3]
	global_load_dwordx4 v[2:5], v[8:9], off offset:64
	global_load_dwordx4 v[10:13], v[8:9], off
	global_load_dwordx4 v[22:25], v[6:7], off offset:128
	v_mul_u32_u24_e32 v6, 0x1c72, v0
	v_mul_u32_u24_e32 v78, 0x195, v0
	s_movk_i32 s2, 0xffee
	s_add_i32 s29, s29, -5
	s_add_i32 s30, s28, -5
	v_lshrrev_b32_e32 v77, 16, v6
	v_mul_i32_i24_sdwa v6, v78, s2 dst_sel:DWORD dst_unused:UNUSED_PAD src0_sel:WORD_1 src1_sel:DWORD
	v_add_u32_sdwa v14, s29, v78 dst_sel:DWORD dst_unused:UNUSED_PAD src0_sel:DWORD src1_sel:WORD_1
	v_add3_u32 v15, s30, v77, v6
	v_or_b32_e32 v6, v15, v14
	s_movk_i32 s5, 0x80
	v_cmp_gt_u32_e32 vcc, s5, v6
	v_mov_b64_e32 v[6:7], 0
	v_mov_b64_e32 v[8:9], 0
	s_and_saveexec_b64 s[2:3], vcc
	v_lshl_or_b32 v9, v14, 7, v15
	v_mad_i32_i24 v8, v77, -9, v0
	v_mul_lo_u32 v9, v9, s4
	v_lshl_add_u32 v8, v8, 3, v9
	v_ashrrev_i32_e32 v9, 31, v8
	s_or_b64 exec, exec, s[2:3]
	v_lshl_add_u64 v[8:9], v[8:9], 1, s[22:23]
	global_load_dwordx4 v[26:29], v[8:9], off
	v_or_b32_e32 v62, 0x200, v0
	v_mul_u32_u24_e32 v8, 0x1c72, v62
	v_lshrrev_b32_e32 v79, 16, v8
	v_mul_u32_u24_e32 v8, 0x653, v62
	v_lshrrev_b32_e32 v80, 18, v8
	v_mul_i32_i24_e32 v9, 0xffffffee, v80
	v_add_u32_e32 v8, s29, v80
	v_add3_u32 v9, s30, v79, v9
	v_or_b32_e32 v14, v9, v8
	v_cmp_gt_u32_e64 s[2:3], s5, v14
	s_and_saveexec_b64 s[4:5], s[2:3]
	v_lshl_or_b32 v7, v8, 7, v9
	s_movk_i32 s6, 0x48
	v_mad_i32_i24 v6, v79, -9, v62
	v_mul_lo_u32 v7, v7, s6
	v_lshl_add_u32 v6, v6, 3, v7
	v_ashrrev_i32_e32 v7, 31, v6
	s_or_b64 exec, exec, s[4:5]
	v_lshl_add_u64 v[6:7], v[6:7], 1, s[22:23]
	global_load_dwordx4 v[30:33], v[6:7], off
	v_or_b32_e32 v61, 0x400, v0
	v_mul_u32_u24_e32 v6, 0x1c72, v61
	v_lshrrev_b32_e32 v81, 16, v6
	v_mul_u32_u24_e32 v6, 0x653, v61
	v_lshrrev_b32_e32 v82, 18, v6
	v_mul_i32_i24_e32 v6, 0xffffffee, v82
	v_add_u32_e32 v14, s29, v82
	v_add3_u32 v15, s30, v81, v6
	v_or_b32_e32 v6, v15, v14
	s_movk_i32 s8, 0x80
	v_cmp_gt_u32_e64 s[4:5], s8, v6
	v_mov_b64_e32 v[6:7], 0
	v_mov_b64_e32 v[8:9], 0
	s_and_saveexec_b64 s[6:7], s[4:5]
	v_lshl_or_b32 v9, v14, 7, v15
	s_movk_i32 s9, 0x48
	v_mad_i32_i24 v8, v81, -9, v61
	v_mul_lo_u32 v9, v9, s9
	v_lshl_add_u32 v8, v8, 3, v9
	v_mov_b32_e32 v9, 0
	s_or_b64 exec, exec, s[6:7]
	v_lshl_add_u64 v[8:9], v[8:9], 1, s[22:23]
	global_load_dwordx4 v[34:37], v[8:9], off
	v_or_b32_e32 v83, 0x600, v0
	v_mul_u32_u24_e32 v8, 0x1c72, v83
	v_lshrrev_b32_e32 v84, 16, v8
	v_mul_u32_u24_e32 v8, 0x653, v83
	v_lshrrev_b32_e32 v85, 18, v8
	v_mul_i32_i24_e32 v9, 0xffffffee, v85
	v_add_u32_e32 v8, s29, v85
	v_add3_u32 v9, s30, v84, v9
	v_or_b32_e32 v14, v9, v8
	v_cmp_gt_u32_e64 s[8:9], s8, v14
	s_and_saveexec_b64 s[6:7], s[8:9]
	v_lshl_or_b32 v7, v8, 7, v9
	s_movk_i32 s10, 0x48
	v_mad_i32_i24 v6, v84, -9, v83
	v_mul_lo_u32 v7, v7, s10
	v_lshl_add_u32 v6, v6, 3, v7
	v_mov_b32_e32 v7, 0
	s_or_b64 exec, exec, s[6:7]
	v_lshl_add_u64 v[6:7], v[6:7], 1, s[22:23]
	global_load_dwordx4 v[42:45], v[6:7], off
	v_or_b32_e32 v86, 0x800, v0
	v_mul_u32_u24_e32 v6, 0x1c72, v86
	v_lshrrev_b32_e32 v14, 16, v6
	v_mul_u32_u24_e32 v6, 0xca5, v86
	s_load_dwordx8 s[12:19], s[0:1], 0x28
	s_load_dwordx2 s[20:21], s[0:1], 0x18
	v_lshrrev_b32_e32 v6, 19, v6
	v_mul_i32_i24_e32 v7, 0xffffffee, v6
	v_add_u32_e32 v15, s29, v6
	v_add3_u32 v16, s30, v14, v7
	v_or_b32_e32 v6, v16, v15
	s_movk_i32 s26, 0x80
	v_cmp_gt_u32_e64 s[10:11], s26, v6
	v_mov_b64_e32 v[6:7], 0
	v_mov_b64_e32 v[8:9], 0
	s_and_saveexec_b64 s[6:7], s[10:11]
	v_lshl_or_b32 v9, v15, 7, v16
	s_movk_i32 s24, 0x48
	v_mad_i32_i24 v8, v14, -9, v86
	v_mul_lo_u32 v9, v9, s24
	v_lshl_add_u32 v8, v8, 3, v9
	v_mov_b32_e32 v9, 0
	s_or_b64 exec, exec, s[6:7]
	v_lshl_add_u64 v[8:9], v[8:9], 1, s[22:23]
	global_load_dwordx4 v[46:49], v[8:9], off
	v_or_b32_e32 v87, 0xa00, v0
	v_min_u32_e32 v8, 0xb63, v87
	v_mul_u32_u24_e32 v14, 0xca5, v8
	s_load_dwordx2 s[24:25], s[0:1], 0x10
	s_load_dwordx2 s[64:65], s[0:1], 0x48
	v_mul_u32_u24_e32 v9, 0x1c72, v8
	v_lshrrev_b32_e32 v14, 19, v14
	v_lshrrev_b32_e32 v9, 16, v9
	v_mul_i32_i24_e32 v15, 0xffffffee, v14
	v_add_u32_e32 v14, s29, v14
	v_add3_u32 v15, s30, v9, v15
	v_or_b32_e32 v16, v15, v14
	v_and_b32_e32 v59, 15, v0
	v_cmp_gt_u32_e64 s[6:7], s26, v16
	s_and_saveexec_b64 s[26:27], s[6:7]
	v_lshl_or_b32 v7, v14, 7, v15
	s_movk_i32 s31, 0x48
	v_mad_i32_i24 v6, v9, -9, v8
	v_mul_lo_u32 v7, v7, s31
	v_lshl_add_u32 v6, v6, 3, v7
	v_mov_b32_e32 v7, 0
	s_or_b64 exec, exec, s[26:27]
	v_lshl_add_u64 v[6:7], v[6:7], 1, s[22:23]
	s_movk_i32 s22, 0xe39
	global_load_dwordx4 v[38:41], v[6:7], off
	v_mul_u32_u24_sdwa v6, v0, s22 dst_sel:DWORD dst_unused:UNUSED_PAD src0_sel:WORD_0 src1_sel:DWORD
	v_lshrrev_b32_e32 v75, 16, v6
	v_or_b32_e32 v14, 0x200, v0
	s_movk_i32 s22, 0xffee
	s_movk_i32 s23, 0x48
	v_mul_u32_u24_e32 v6, 0x48, v75
	v_mul_u32_u24_e32 v8, 0xe39, v14
	v_mad_i32_i24 v53, v75, s22, v0
	v_lshlrev_b32_e32 v50, 2, v6
	v_mov_b32_e32 v51, 0
	v_mul_i32_i24_sdwa v15, v8, s22 dst_sel:DWORD dst_unused:UNUSED_PAD src0_sel:WORD_1 src1_sel:DWORD
	v_mul_u32_u24_sdwa v8, v8, s23 dst_sel:DWORD dst_unused:UNUSED_PAD src0_sel:WORD_1 src1_sel:DWORD
	s_waitcnt lgkmcnt(0)
	v_lshl_add_u64 v[6:7], s[24:25], 0, v[50:51]
	v_lshlrev_b32_e32 v54, 2, v53
	v_lshlrev_b32_e32 v50, 2, v8
	v_add_lshl_u32 v14, v15, v14, 2
	v_ashrrev_i32_e32 v55, 31, v54
	v_lshl_add_u64 v[8:9], s[24:25], 0, v[50:51]
	v_ashrrev_i32_e32 v15, 31, v14
	v_lshl_add_u64 v[6:7], v[54:55], 2, v[6:7]
	v_lshl_add_u64 v[8:9], v[14:15], 2, v[8:9]
	global_load_dwordx4 v[18:21], v[6:7], off
	global_load_dwordx4 v[14:17], v[8:9], off
	v_min_u32_e32 v8, 0x50f, v61
	v_mul_u32_u24_e32 v6, 0xe39, v8
	v_mul_i32_i24_sdwa v9, v6, s22 dst_sel:DWORD dst_unused:UNUSED_PAD src0_sel:WORD_1 src1_sel:DWORD
	v_mul_u32_u24_sdwa v6, v6, s23 dst_sel:DWORD dst_unused:UNUSED_PAD src0_sel:WORD_1 src1_sel:DWORD
	v_lshlrev_b32_e32 v50, 2, v6
	v_lshl_add_u64 v[6:7], s[24:25], 0, v[50:51]
	v_min_u32_e32 v50, 0x47, v0
	v_add_lshl_u32 v8, v9, v8, 2
	v_lshlrev_b32_e32 v50, 2, v50
	v_add_u32_e32 v63, -8, v59
	v_ashrrev_i32_e32 v9, 31, v8
	global_load_dword v68, v50, s[20:21]
	v_min_u32_e32 v50, 6, v59
	v_med3_i32 v64, v63, 0, 2
	v_mul_u32_u24_e32 v52, 7, v52
	v_and_b32_e32 v72, 15, v62
	v_lshl_add_u64 v[6:7], v[8:9], 2, v[6:7]
	v_lshlrev_b32_e32 v55, 2, v50
	v_lshlrev_b32_e32 v65, 2, v64
	v_add_lshl_u32 v50, v52, v50, 2
	v_lshrrev_b32_e32 v52, 4, v62
	v_add_u32_e32 v71, -8, v72
	global_load_dwordx4 v[6:9], v[6:7], off
	v_med3_i32 v67, v71, 0, 2
	global_load_dword v55, v55, s[14:15]
	s_nop 0
	global_load_dword v64, v65, s[18:19]
	global_load_dword v70, v65, s[16:17]
	v_min_u32_e32 v65, 6, v72
	v_mul_u32_u24_e32 v52, 7, v52
	v_add_lshl_u32 v52, v52, v65, 2
	global_load_dword v66, v50, s[12:13]
	global_load_dword v65, v52, s[12:13]
	v_mad_u32_u24 v50, 64, 3, v67
	v_add_u32_e32 v50, 0xffffff40, v50
	v_lshl_add_u64 v[88:89], v[50:51], 2, s[16:17]
	v_min_u32_e32 v50, 0x47f, v61
	v_lshrrev_b32_e32 v52, 4, v50
	v_and_b32_e32 v50, 15, v50
	v_add_u32_e32 v69, -8, v50
	s_movk_i32 s14, 0xff40
	v_min_u32_e32 v67, 6, v50
	v_med3_i32 v50, v69, 0, 2
	v_mul_u32_u24_e32 v52, 3, v52
	v_add3_u32 v50, v52, v50, s14
	global_load_dword v74, v[88:89], off
	v_lshlrev_b32_e32 v67, 2, v67
	v_lshl_add_u64 v[88:89], v[50:51], 2, s[16:17]
	global_load_dword v67, v67, s[12:13] offset:1764
	s_movk_i32 s12, 0x144
	global_load_dword v73, v[88:89], off
	v_cmp_gt_u32_e64 s[12:13], s12, v0
	s_and_saveexec_b64 s[14:15], s[12:13]
	s_cbranch_execz .LBB2_14
	v_mul_i32_i24_e32 v50, 0x1c72, v53
	v_lshrrev_b32_e32 v52, 31, v50
	v_add_u16_sdwa v50, v50, v52 dst_sel:DWORD dst_unused:UNUSED_PAD src0_sel:WORD_1 src1_sel:DWORD
	v_bfe_i32 v50, v50, 0, 16
	v_mul_i32_i24_e32 v52, -9, v50
	v_mad_u32_u24 v50, v75, 20, v50
	v_mul_i32_i24_e32 v50, 0xa0, v50
	v_add_lshl_u32 v52, v52, v53, 4
	v_add3_u32 v88, v50, 0, v52
	v_mov_b32_e32 v50, v51
	v_mov_b32_e32 v52, v51
	v_mov_b32_e32 v53, v51
	ds_write_b128 v88, v[50:53] offset:2880
